# v69 plus grid barrier: last XCD leader bumps every XCD generation word itself, other leaders wait on their own word (one hop less)
# speedup vs baseline: 1.0060x; 1.0002x over previous
; __device__ __forceinline__ unsigned xb_ld(unsigned* p)              { return __hip_atomic_load(p, __ATOMIC_RELAXED, __HIP_MEMORY_SCOPE_AGENT); }
; __device__ __forceinline__ unsigned xb_add(unsigned* p, unsigned v) { return __hip_atomic_fetch_add(p, v, __ATOMIC_RELAXED, __HIP_MEMORY_SCOPE_AGENT); }
; #define XB_SPIN(cond, bar) do { unsigned _sp = 0; while (cond) { __builtin_amdgcn_s_sleep(1); \
;     if ((++_sp & 255u) == 0u) { if (xb_ld(&(bar)[XB_TMO])) break; if (_sp > XB_SPIN_CAP) { atomicAdd(&(bar)[XB_TMO], 1u); break; } } } } while (0)
; __device__ __forceinline__ void xcd_barrier(const XcdBarrier& b) {
;     ...
;         const unsigned old = xb_add(&bar[XB_XSUB(b.x)], 1u);
;         const unsigned gen = old / nloc;
;         if (old + 1u == (gen + 1u) * nloc) {
;             __builtin_amdgcn_fence(__ATOMIC_RELEASE, "agent");
;             asm volatile("s_waitcnt vmcnt(0)" ::: "memory");
;             const unsigned og = xb_add(&bar[XB_TOP], 1u);
;             const unsigned tg = og / nx;
;             if (og + 1u == (tg + 1u) * nx) xb_add(&bar[XB_TOPGEN], 1u);
;             else XB_SPIN(xb_ld(&bar[XB_TOPGEN]) == tg, bar);
;             __builtin_amdgcn_fence(__ATOMIC_ACQUIRE, "agent");
;             xb_add(&bar[XB_XGEN(b.x)], 1u);
;             asm volatile("s_waitcnt vmcnt(0)" ::: "memory");
;         } else {
;             XB_SPIN(xb_ld(&bar[XB_XGEN(b.x)]) == gen, bar);
.LBB0_286:
	s_or_b64 exec, exec, s[4:5]
	v_cvt_f32_u32_e32 v4, v2
	s_waitcnt vmcnt(0)
	v_readfirstlane_b32 s2, v3
	s_mov_b64 s[4:5], -1
	v_rcp_iflag_f32_e32 v4, v4
	v_add_u32_e32 v0, s2, v0
	v_add_u32_e32 v5, 1, v0
	v_readlane_b32 s2, v252, 7
	v_mul_f32_e32 v3, 0x4f7ffffe, v4
	v_cvt_u32_f32_e32 v3, v3
	v_sub_u32_e32 v4, 0, v2
	v_readlane_b32 s3, v252, 8
	v_mul_lo_u32 v4, v4, v3
	v_mul_hi_u32 v4, v3, v4
	v_add_u32_e32 v3, v3, v4
	v_mul_hi_u32 v3, v0, v3
	v_mul_lo_u32 v4, v3, v2
	v_sub_u32_e32 v0, v0, v4
	v_add_u32_e32 v6, 1, v3
	v_cmp_ge_u32_e32 vcc, v0, v2
	v_sub_u32_e32 v4, v0, v2
	s_nop 0
	v_cndmask_b32_e32 v3, v3, v6, vcc
	v_cndmask_b32_e32 v0, v0, v4, vcc
	v_add_u32_e32 v4, 1, v3
	v_cmp_ge_u32_e32 vcc, v0, v2
	s_nop 1
	v_cndmask_b32_e32 v0, v3, v4, vcc
	v_mul_lo_u32 v3, v2, v0
	v_add_u32_e32 v2, v3, v2
	v_cmp_ne_u32_e32 vcc, v5, v2
	v_mov_b64_e32 v[2:3], s[2:3]
	s_and_saveexec_b64 s[2:3], vcc
	s_cbranch_execz .LBB0_298
	v_readlane_b32 s4, v252, 3
	v_readlane_b32 s5, v252, 4
	s_mov_b64 s[6:7], 0
	s_nop 3
	global_load_dword v2, v1, s[4:5] sc1
	s_waitcnt vmcnt(0)
	v_cmp_eq_u32_e32 vcc, v2, v0
	s_and_saveexec_b64 s[4:5], vcc
	s_cbranch_execz .LBB0_297
	s_mov_b32 s17, 1
	s_branch .LBB0_290

; __device__ __forceinline__ unsigned xb_ld(unsigned* p)              { return __hip_atomic_load(p, __ATOMIC_RELAXED, __HIP_MEMORY_SCOPE_AGENT); }
; __device__ __forceinline__ unsigned xb_add(unsigned* p, unsigned v) { return __hip_atomic_fetch_add(p, v, __ATOMIC_RELAXED, __HIP_MEMORY_SCOPE_AGENT); }
; #define XB_SPIN(cond, bar) do { unsigned _sp = 0; while (cond) { __builtin_amdgcn_s_sleep(1); \
;     if ((++_sp & 255u) == 0u) { if (xb_ld(&(bar)[XB_TMO])) break; if (_sp > XB_SPIN_CAP) { atomicAdd(&(bar)[XB_TMO], 1u); break; } } } } while (0)
; __device__ __forceinline__ void xcd_barrier(const XcdBarrier& b) {
;     ...
;             const unsigned og = xb_add(&bar[XB_TOP], 1u);
;             const unsigned tg = og / nx;
;             if (og + 1u == (tg + 1u) * nx) xb_add(&bar[XB_TOPGEN], 1u);
;             else XB_SPIN(xb_ld(&bar[XB_TOPGEN]) == tg, bar);
;             __builtin_amdgcn_fence(__ATOMIC_ACQUIRE, "agent");
;             xb_add(&bar[XB_XGEN(b.x)], 1u);
.LBB0_298:
	s_or_b64 exec, exec, s[2:3]
	s_and_saveexec_b64 s[2:3], s[4:5]
	s_cbranch_execz .LBB0_300
	v_mov_b32_e32 v0, 1
	global_atomic_add v[2:3], v0, off
	v_readlane_b32 s6, v253, 52
	v_readlane_b32 s7, v253, 53
	s_add_u32 s6, s6, 0x2400
	s_addc_u32 s7, s7, 0
	global_atomic_add v1, v0, s[6:7]
	global_atomic_add v1, v0, s[6:7] offset:256
	global_atomic_add v1, v0, s[6:7] offset:512
	global_atomic_add v1, v0, s[6:7] offset:768
	global_atomic_add v1, v0, s[6:7] offset:1024
	global_atomic_add v1, v0, s[6:7] offset:1280
	global_atomic_add v1, v0, s[6:7] offset:1536
	global_atomic_add v1, v0, s[6:7] offset:1792
	global_atomic_add v1, v0, s[6:7] offset:2048
	global_atomic_add v1, v0, s[6:7] offset:2304
	global_atomic_add v1, v0, s[6:7] offset:2560
	global_atomic_add v1, v0, s[6:7] offset:2816
	global_atomic_add v1, v0, s[6:7] offset:3072
	global_atomic_add v1, v0, s[6:7] offset:3328
	global_atomic_add v1, v0, s[6:7] offset:3584
	global_atomic_add v1, v0, s[6:7] offset:3840
.LBB0_300:
	s_or_b64 exec, exec, s[2:3]
	v_readlane_b32 s2, v252, 3
	v_readlane_b32 s3, v252, 4
	v_mov_b32_e32 v0, 1
	s_waitcnt vmcnt(0)
	s_nop 2
	buffer_inv sc1
	s_waitcnt vmcnt(0)

; __device__ __forceinline__ unsigned xb_ld(unsigned* p)              { return __hip_atomic_load(p, __ATOMIC_RELAXED, __HIP_MEMORY_SCOPE_AGENT); }
; __device__ __forceinline__ unsigned xb_add(unsigned* p, unsigned v) { return __hip_atomic_fetch_add(p, v, __ATOMIC_RELAXED, __HIP_MEMORY_SCOPE_AGENT); }
; #define XB_SPIN(cond, bar) do { unsigned _sp = 0; while (cond) { __builtin_amdgcn_s_sleep(1); \
;     if ((++_sp & 255u) == 0u) { if (xb_ld(&(bar)[XB_TMO])) break; if (_sp > XB_SPIN_CAP) { atomicAdd(&(bar)[XB_TMO], 1u); break; } } } } while (0)
; __device__ __forceinline__ void xcd_barrier(const XcdBarrier& b) {
;     ...
;         const unsigned old = xb_add(&bar[XB_XSUB(b.x)], 1u);
;         const unsigned gen = old / nloc;
;         if (old + 1u == (gen + 1u) * nloc) {
;             __builtin_amdgcn_fence(__ATOMIC_RELEASE, "agent");
;             asm volatile("s_waitcnt vmcnt(0)" ::: "memory");
;             const unsigned og = xb_add(&bar[XB_TOP], 1u);
;             const unsigned tg = og / nx;
;             if (og + 1u == (tg + 1u) * nx) xb_add(&bar[XB_TOPGEN], 1u);
;             else XB_SPIN(xb_ld(&bar[XB_TOPGEN]) == tg, bar);
;             __builtin_amdgcn_fence(__ATOMIC_ACQUIRE, "agent");
;             xb_add(&bar[XB_XGEN(b.x)], 1u);
;             asm volatile("s_waitcnt vmcnt(0)" ::: "memory");
;         } else {
;             XB_SPIN(xb_ld(&bar[XB_XGEN(b.x)]) == gen, bar);
.LBB0_455:
	s_or_b64 exec, exec, s[4:5]
	s_waitcnt vmcnt(0)
	v_readfirstlane_b32 s2, v3
	v_sub_u32_e32 v4, 0, v2
	s_mov_b64 s[4:5], -1
	v_add_u32_e32 v3, s2, v0
	v_cvt_f32_u32_e32 v0, v2
	v_readlane_b32 s2, v252, 7
	v_readlane_b32 s3, v252, 8
	v_rcp_iflag_f32_e32 v0, v0
	s_nop 0
	v_mul_f32_e32 v0, 0x4f7ffffe, v0
	v_cvt_u32_f32_e32 v0, v0
	v_mul_lo_u32 v4, v4, v0
	v_mul_hi_u32 v4, v0, v4
	v_add_u32_e32 v0, v0, v4
	v_mul_hi_u32 v0, v3, v0
	v_mul_lo_u32 v4, v0, v2
	v_sub_u32_e32 v4, v3, v4
	v_cmp_ge_u32_e32 vcc, v4, v2
	v_add_u32_e32 v5, 1, v0
	v_add_u32_e32 v3, 1, v3
	v_cndmask_b32_e32 v0, v0, v5, vcc
	v_sub_u32_e32 v5, v4, v2
	v_cndmask_b32_e32 v4, v4, v5, vcc
	v_cmp_ge_u32_e32 vcc, v4, v2
	v_add_u32_e32 v4, 1, v0
	s_nop 0
	v_cndmask_b32_e32 v0, v0, v4, vcc
	v_mul_lo_u32 v4, v2, v0
	v_add_u32_e32 v2, v4, v2
	v_cmp_ne_u32_e32 vcc, v3, v2
	v_mov_b64_e32 v[2:3], s[2:3]
	s_and_saveexec_b64 s[2:3], vcc
	s_cbranch_execz .LBB0_467
	v_readlane_b32 s4, v252, 3
	v_readlane_b32 s5, v252, 4
	s_mov_b64 s[6:7], 0
	s_nop 3
	global_load_dword v2, v1, s[4:5] sc1
	s_waitcnt vmcnt(0)
	v_cmp_eq_u32_e32 vcc, v2, v0
	s_and_saveexec_b64 s[4:5], vcc
	s_cbranch_execz .LBB0_466
	s_mov_b32 s21, 1
	s_branch .LBB0_459

; __device__ __forceinline__ unsigned xb_ld(unsigned* p)              { return __hip_atomic_load(p, __ATOMIC_RELAXED, __HIP_MEMORY_SCOPE_AGENT); }
; __device__ __forceinline__ unsigned xb_add(unsigned* p, unsigned v) { return __hip_atomic_fetch_add(p, v, __ATOMIC_RELAXED, __HIP_MEMORY_SCOPE_AGENT); }
; #define XB_SPIN(cond, bar) do { unsigned _sp = 0; while (cond) { __builtin_amdgcn_s_sleep(1); \
;     if ((++_sp & 255u) == 0u) { if (xb_ld(&(bar)[XB_TMO])) break; if (_sp > XB_SPIN_CAP) { atomicAdd(&(bar)[XB_TMO], 1u); break; } } } } while (0)
; __device__ __forceinline__ void xcd_barrier(const XcdBarrier& b) {
;     ...
;         const unsigned old = xb_add(&bar[XB_XSUB(b.x)], 1u);
;         const unsigned gen = old / nloc;
;         if (old + 1u == (gen + 1u) * nloc) {
;             __builtin_amdgcn_fence(__ATOMIC_RELEASE, "agent");
;             asm volatile("s_waitcnt vmcnt(0)" ::: "memory");
;             const unsigned og = xb_add(&bar[XB_TOP], 1u);
;             const unsigned tg = og / nx;
;             if (og + 1u == (tg + 1u) * nx) xb_add(&bar[XB_TOPGEN], 1u);
;             else XB_SPIN(xb_ld(&bar[XB_TOPGEN]) == tg, bar);
;             __builtin_amdgcn_fence(__ATOMIC_ACQUIRE, "agent");
;             xb_add(&bar[XB_XGEN(b.x)], 1u);
;             asm volatile("s_waitcnt vmcnt(0)" ::: "memory");
;         } else {
;             XB_SPIN(xb_ld(&bar[XB_XGEN(b.x)]) == gen, bar);
.LBB0_537:
	s_or_b64 exec, exec, s[4:5]
	s_waitcnt vmcnt(0)
	v_readfirstlane_b32 s2, v3
	v_sub_u32_e32 v4, 0, v2
	s_mov_b64 s[4:5], -1
	v_add_u32_e32 v3, s2, v0
	v_cvt_f32_u32_e32 v0, v2
	v_readlane_b32 s2, v252, 7
	v_readlane_b32 s3, v252, 8
	v_rcp_iflag_f32_e32 v0, v0
	s_nop 0
	v_mul_f32_e32 v0, 0x4f7ffffe, v0
	v_cvt_u32_f32_e32 v0, v0
	v_mul_lo_u32 v4, v4, v0
	v_mul_hi_u32 v4, v0, v4
	v_add_u32_e32 v0, v0, v4
	v_mul_hi_u32 v0, v3, v0
	v_mul_lo_u32 v4, v0, v2
	v_sub_u32_e32 v4, v3, v4
	v_cmp_ge_u32_e32 vcc, v4, v2
	v_add_u32_e32 v5, 1, v0
	v_add_u32_e32 v3, 1, v3
	v_cndmask_b32_e32 v0, v0, v5, vcc
	v_sub_u32_e32 v5, v4, v2
	v_cndmask_b32_e32 v4, v4, v5, vcc
	v_cmp_ge_u32_e32 vcc, v4, v2
	v_add_u32_e32 v4, 1, v0
	s_nop 0
	v_cndmask_b32_e32 v0, v0, v4, vcc
	v_mul_lo_u32 v4, v2, v0
	v_add_u32_e32 v2, v4, v2
	v_cmp_ne_u32_e32 vcc, v3, v2
	v_mov_b64_e32 v[2:3], s[2:3]
	s_and_saveexec_b64 s[2:3], vcc
	s_cbranch_execz .LBB0_549
	v_readlane_b32 s4, v252, 3
	v_readlane_b32 s5, v252, 4
	s_mov_b64 s[6:7], 0
	s_nop 3
	global_load_dword v2, v1, s[4:5] sc1
	s_waitcnt vmcnt(0)
	v_cmp_eq_u32_e32 vcc, v2, v0
	s_and_saveexec_b64 s[4:5], vcc
	s_cbranch_execz .LBB0_548
	s_mov_b32 s17, 1
	s_branch .LBB0_541

; __device__ __forceinline__ unsigned xb_ld(unsigned* p)              { return __hip_atomic_load(p, __ATOMIC_RELAXED, __HIP_MEMORY_SCOPE_AGENT); }
; __device__ __forceinline__ unsigned xb_add(unsigned* p, unsigned v) { return __hip_atomic_fetch_add(p, v, __ATOMIC_RELAXED, __HIP_MEMORY_SCOPE_AGENT); }
; #define XB_SPIN(cond, bar) do { unsigned _sp = 0; while (cond) { __builtin_amdgcn_s_sleep(1); \
;     if ((++_sp & 255u) == 0u) { if (xb_ld(&(bar)[XB_TMO])) break; if (_sp > XB_SPIN_CAP) { atomicAdd(&(bar)[XB_TMO], 1u); break; } } } } while (0)
; __device__ __forceinline__ void xcd_barrier(const XcdBarrier& b) {
;     ...
;         const unsigned old = xb_add(&bar[XB_XSUB(b.x)], 1u);
;         const unsigned gen = old / nloc;
;         if (old + 1u == (gen + 1u) * nloc) {
;             __builtin_amdgcn_fence(__ATOMIC_RELEASE, "agent");
;             asm volatile("s_waitcnt vmcnt(0)" ::: "memory");
;             const unsigned og = xb_add(&bar[XB_TOP], 1u);
;             const unsigned tg = og / nx;
;             if (og + 1u == (tg + 1u) * nx) xb_add(&bar[XB_TOPGEN], 1u);
;             else XB_SPIN(xb_ld(&bar[XB_TOPGEN]) == tg, bar);
;             __builtin_amdgcn_fence(__ATOMIC_ACQUIRE, "agent");
;             xb_add(&bar[XB_XGEN(b.x)], 1u);
;             asm volatile("s_waitcnt vmcnt(0)" ::: "memory");
;         } else {
;             XB_SPIN(xb_ld(&bar[XB_XGEN(b.x)]) == gen, bar);
.LBB0_1488:
	s_or_b64 exec, exec, s[4:5]
	s_waitcnt vmcnt(0)
	v_readfirstlane_b32 s2, v3
	v_sub_u32_e32 v4, 0, v2
	s_mov_b64 s[4:5], -1
	v_add_u32_e32 v3, s2, v0
	v_cvt_f32_u32_e32 v0, v2
	v_readlane_b32 s2, v252, 7
	v_readlane_b32 s3, v252, 8
	v_rcp_iflag_f32_e32 v0, v0
	s_nop 0
	v_mul_f32_e32 v0, 0x4f7ffffe, v0
	v_cvt_u32_f32_e32 v0, v0
	v_mul_lo_u32 v4, v4, v0
	v_mul_hi_u32 v4, v0, v4
	v_add_u32_e32 v0, v0, v4
	v_mul_hi_u32 v0, v3, v0
	v_mul_lo_u32 v4, v0, v2
	v_sub_u32_e32 v4, v3, v4
	v_cmp_ge_u32_e32 vcc, v4, v2
	v_add_u32_e32 v5, 1, v0
	v_add_u32_e32 v3, 1, v3
	v_cndmask_b32_e32 v0, v0, v5, vcc
	v_sub_u32_e32 v5, v4, v2
	v_cndmask_b32_e32 v4, v4, v5, vcc
	v_cmp_ge_u32_e32 vcc, v4, v2
	v_add_u32_e32 v4, 1, v0
	s_nop 0
	v_cndmask_b32_e32 v0, v0, v4, vcc
	v_mul_lo_u32 v4, v2, v0
	v_add_u32_e32 v2, v4, v2
	v_cmp_ne_u32_e32 vcc, v3, v2
	v_mov_b64_e32 v[2:3], s[2:3]
	s_and_saveexec_b64 s[2:3], vcc
	s_cbranch_execz .LBB0_1500
	v_readlane_b32 s4, v252, 3
	v_readlane_b32 s5, v252, 4
	s_mov_b64 s[6:7], 0
	s_nop 3
	global_load_dword v2, v1, s[4:5] sc1
	s_waitcnt vmcnt(0)
	v_cmp_eq_u32_e32 vcc, v2, v0
	s_and_saveexec_b64 s[4:5], vcc
	s_cbranch_execz .LBB0_1499
	s_mov_b32 s16, 1
	s_branch .LBB0_1492
